# t14
# speedup vs baseline: 1.0119x; 1.0119x over previous
.Ljoin:
	s_barrier
	v_mov_b32_e32 v6, 0x6000
	ds_read_b96 v[32:34], v6
	ds_read_b96 v[36:38], v6 offset:16
	ds_read_b96 v[40:42], v6 offset:32
	ds_read_b96 v[44:46], v6 offset:48
	v_add_u32_e32 v56, 0xc00, v3
	v_add_u32_e32 v57, 0x1200, v3
	ds_read2_b32 v[8:9], v3 offset0:0 offset1:1
	ds_read_b32 v24, v3 offset:8
	ds_read2_b32 v[10:11], v3 offset0:192 offset1:193
	ds_read_b32 v25, v3 offset:776
	ds_read2_b32 v[12:13], v4 offset0:0 offset1:1
	ds_read_b32 v26, v4 offset:8
	s_waitcnt lgkmcnt(4)
	v_fma_f32 v60, v8, v32, v44
	v_fma_f32 v61, v8, v33, v45
	v_fma_f32 v62, v8, v34, v46
	v_fmac_f32_e32 v60, v9, v36
	v_fmac_f32_e32 v61, v9, v37
	v_fmac_f32_e32 v62, v9, v38
	v_fmac_f32_e32 v60, v24, v40
	v_fmac_f32_e32 v61, v24, v41
	v_fmac_f32_e32 v62, v24, v42
	ds_write2_b32 v3, v60, v61 offset0:0 offset1:1
	ds_write_b32 v3, v62 offset:8
	ds_read2_b32 v[14:15], v4 offset0:192 offset1:193
	ds_read_b32 v27, v4 offset:776
	s_waitcnt lgkmcnt(6)
	v_fma_f32 v35, v10, v32, v44
	v_fma_f32 v39, v10, v33, v45
	v_fma_f32 v43, v10, v34, v46
	v_fmac_f32_e32 v35, v11, v36
	v_fmac_f32_e32 v39, v11, v37
	v_fmac_f32_e32 v43, v11, v38
	v_fmac_f32_e32 v35, v25, v40
	v_fmac_f32_e32 v39, v25, v41
	v_fmac_f32_e32 v43, v25, v42
	ds_write2_b32 v3, v35, v39 offset0:192 offset1:193
	ds_write_b32 v3, v43 offset:776
	ds_read2_b32 v[16:17], v56 offset0:0 offset1:1
	ds_read_b32 v28, v56 offset:8
	s_waitcnt lgkmcnt(8)
	v_fma_f32 v60, v12, v32, v44
	v_fma_f32 v61, v12, v33, v45
	v_fma_f32 v62, v12, v34, v46
	v_fmac_f32_e32 v60, v13, v36
	v_fmac_f32_e32 v61, v13, v37
	v_fmac_f32_e32 v62, v13, v38
	v_fmac_f32_e32 v60, v26, v40
	v_fmac_f32_e32 v61, v26, v41
	v_fmac_f32_e32 v62, v26, v42
	ds_write2_b32 v4, v60, v61 offset0:0 offset1:1
	ds_write_b32 v4, v62 offset:8
	ds_read2_b32 v[18:19], v56 offset0:192 offset1:193
	ds_read_b32 v29, v56 offset:776
	s_waitcnt lgkmcnt(8)
	v_fma_f32 v35, v14, v32, v44
	v_fma_f32 v39, v14, v33, v45
	v_fma_f32 v43, v14, v34, v46
	v_fmac_f32_e32 v35, v15, v36
	v_fmac_f32_e32 v39, v15, v37
	v_fmac_f32_e32 v43, v15, v38
	v_fmac_f32_e32 v35, v27, v40
	v_fmac_f32_e32 v39, v27, v41
	v_fmac_f32_e32 v43, v27, v42
	ds_write2_b32 v4, v35, v39 offset0:192 offset1:193
	ds_write_b32 v4, v43 offset:776
	ds_read2_b32 v[20:21], v57 offset0:0 offset1:1
	ds_read_b32 v30, v57 offset:8
	s_waitcnt lgkmcnt(8)
	v_fma_f32 v60, v16, v32, v44
	v_fma_f32 v61, v16, v33, v45
	v_fma_f32 v62, v16, v34, v46
	v_fmac_f32_e32 v60, v17, v36
	v_fmac_f32_e32 v61, v17, v37
	v_fmac_f32_e32 v62, v17, v38
	v_fmac_f32_e32 v60, v28, v40
	v_fmac_f32_e32 v61, v28, v41
	v_fmac_f32_e32 v62, v28, v42
	ds_write2_b32 v56, v60, v61 offset0:0 offset1:1
	ds_write_b32 v56, v62 offset:8
	ds_read2_b32 v[22:23], v57 offset0:192 offset1:193
	ds_read_b32 v31, v57 offset:776
	s_waitcnt lgkmcnt(8)
	v_fma_f32 v35, v18, v32, v44
	v_fma_f32 v39, v18, v33, v45
	v_fma_f32 v43, v18, v34, v46
	v_fmac_f32_e32 v35, v19, v36
	v_fmac_f32_e32 v39, v19, v37
	v_fmac_f32_e32 v43, v19, v38
	v_fmac_f32_e32 v35, v29, v40
	v_fmac_f32_e32 v39, v29, v41
	v_fmac_f32_e32 v43, v29, v42
	ds_write2_b32 v56, v35, v39 offset0:192 offset1:193
	ds_write_b32 v56, v43 offset:776
	s_waitcnt lgkmcnt(6)
	v_fma_f32 v60, v20, v32, v44
	v_fma_f32 v61, v20, v33, v45
	v_fma_f32 v62, v20, v34, v46
	v_fmac_f32_e32 v60, v21, v36
	v_fmac_f32_e32 v61, v21, v37
	v_fmac_f32_e32 v62, v21, v38
	v_fmac_f32_e32 v60, v30, v40
	v_fmac_f32_e32 v61, v30, v41
	v_fmac_f32_e32 v62, v30, v42
	ds_write2_b32 v57, v60, v61 offset0:0 offset1:1
	ds_write_b32 v57, v62 offset:8
	s_waitcnt lgkmcnt(4)
	v_fma_f32 v35, v22, v32, v44
	v_fma_f32 v39, v22, v33, v45
	v_fma_f32 v43, v22, v34, v46
	v_fmac_f32_e32 v35, v23, v36
	v_fmac_f32_e32 v39, v23, v37
	v_fmac_f32_e32 v43, v23, v38
	v_fmac_f32_e32 v35, v31, v40
	v_fmac_f32_e32 v39, v31, v41
	v_fmac_f32_e32 v43, v31, v42
	ds_write2_b32 v57, v35, v39 offset0:192 offset1:193
	ds_write_b32 v57, v43 offset:776
	ds_read_b128 v[8:11], v2
	ds_read_b128 v[12:15], v2 offset:1024
	ds_read_b128 v[16:19], v2 offset:2048
	ds_read_b128 v[20:23], v2 offset:3072
	ds_read_b128 v[24:27], v2 offset:4096
	ds_read_b128 v[28:31], v2 offset:5120
	s_waitcnt lgkmcnt(5)
	global_store_dwordx4 v1, v[8:11], s[10:11] offset:-2048 sc0 sc1 nt
	s_waitcnt lgkmcnt(4)
	global_store_dwordx4 v1, v[12:15], s[10:11] offset:-1024 sc0 sc1 nt
	s_waitcnt lgkmcnt(3)
	global_store_dwordx4 v1, v[16:19], s[10:11] offset:0 sc0 sc1 nt
	s_waitcnt lgkmcnt(2)
	global_store_dwordx4 v1, v[20:23], s[10:11] offset:1024 sc0 sc1 nt
	s_waitcnt lgkmcnt(1)
	global_store_dwordx4 v1, v[24:27], s[10:11] offset:2048 sc0 sc1 nt
	s_waitcnt lgkmcnt(0)
	s_and_saveexec_b64 s[16:17], s[14:15]
	global_store_dwordx4 v1, v[28:31], s[10:11] offset:3072 sc0 sc1 nt
	s_endpgm
